# baseline (speedup 1.0000x reference)
.LBB3_347:
	v_mov_b32_e32 v219, s49
	ds_read_b128 v[220:223], v219
	s_lshl_b64 s[6:7], s[28:29], 11
	v_mov_b32_e32 v90, 0
	v_mov_b32_e32 v98, 0
	v_mov_b32_e32 v99, 0
	s_waitcnt lgkmcnt(0)
	v_readfirstlane_b32 s22, v220
	v_mov_b32_e32 v100, 0
	v_mov_b32_e32 v101, 0
	v_mov_b32_e32 v18, 0
	v_mov_b32_e32 v19, 0
	v_mov_b32_e32 v20, 0
	v_mov_b32_e32 v21, 0
	s_and_saveexec_b64 s[28:29], s[0:1]
	s_cbranch_execz .LBB3_349
	s_ashr_i32 s27, s22, 31
	s_add_u32 s22, s6, s22
	s_addc_u32 s27, s7, s27
	s_mul_i32 s30, s22, s48
	s_mul_hi_u32 s31, s22, s33
	s_add_i32 s30, s31, s30
	s_mul_i32 s27, s27, s33
	s_add_i32 s31, s30, s27
	s_mul_i32 s30, s22, s33
	s_lshl_b64 s[30:31], s[30:31], 1
	v_lshl_add_u64 v[10:11], v[158:159], 0, s[30:31]
	global_load_dwordx4 v[98:101], v[10:11], off
	v_lshl_add_u64 v[10:11], v[160:161], 0, s[30:31]
	global_load_dwordx4 v[18:21], v[10:11], off
.LBB3_349:
	s_or_b64 exec, exec, s[28:29]
	v_mov_b32_e32 v91, 0
	v_mov_b32_e32 v92, 0
	v_mov_b32_e32 v93, 0
	v_mov_b32_e32 v26, 0
	s_waitcnt lgkmcnt(0)
	v_readfirstlane_b32 s22, v221
	v_mov_b32_e32 v27, 0
	v_mov_b32_e32 v28, 0
	v_mov_b32_e32 v29, 0
	s_and_saveexec_b64 s[28:29], s[0:1]
	s_cbranch_execz .LBB3_351
	s_ashr_i32 s27, s22, 31
	s_add_u32 s22, s6, s22
	s_addc_u32 s27, s7, s27
	s_mul_i32 s30, s22, s48
	s_mul_hi_u32 s31, s22, s33
	s_add_i32 s30, s31, s30
	s_mul_i32 s27, s27, s33
	s_add_i32 s31, s30, s27
	s_mul_i32 s30, s22, s33
	s_lshl_b64 s[30:31], s[30:31], 1
	v_lshl_add_u64 v[10:11], v[158:159], 0, s[30:31]
	global_load_dwordx4 v[90:93], v[10:11], off
	v_lshl_add_u64 v[10:11], v[160:161], 0, s[30:31]
	global_load_dwordx4 v[26:29], v[10:11], off
.LBB3_351:
	s_or_b64 exec, exec, s[28:29]
	v_mov_b32_e32 v106, 0
	v_mov_b32_e32 v114, 0
	v_mov_b32_e32 v115, 0
	v_mov_b32_e32 v116, 0
	s_waitcnt lgkmcnt(0)
	v_readfirstlane_b32 s22, v222
	v_mov_b32_e32 v117, 0
	v_mov_b32_e32 v34, 0
	v_mov_b32_e32 v35, 0
	v_mov_b32_e32 v36, 0
	v_mov_b32_e32 v37, 0
	s_and_saveexec_b64 s[28:29], s[0:1]
	s_cbranch_execz .LBB3_353
	s_ashr_i32 s27, s22, 31
	s_add_u32 s22, s6, s22
	s_addc_u32 s27, s7, s27
	s_mul_i32 s30, s22, s48
	s_mul_hi_u32 s31, s22, s33
	s_add_i32 s30, s31, s30
	s_mul_i32 s27, s27, s33
	s_add_i32 s31, s30, s27
	s_mul_i32 s30, s22, s33
	s_lshl_b64 s[30:31], s[30:31], 1
	v_lshl_add_u64 v[10:11], v[158:159], 0, s[30:31]
	global_load_dwordx4 v[114:117], v[10:11], off
	v_lshl_add_u64 v[10:11], v[160:161], 0, s[30:31]
	global_load_dwordx4 v[34:37], v[10:11], off
.LBB3_353:
	s_or_b64 exec, exec, s[28:29]
	v_mov_b32_e32 v107, 0
	v_mov_b32_e32 v108, 0
	v_mov_b32_e32 v109, 0
	v_mov_b32_e32 v42, 0
	s_waitcnt lgkmcnt(0)
	v_readfirstlane_b32 s22, v223
	ds_read_b128 v[220:223], v219 offset:16
	v_mov_b32_e32 v43, 0
	v_mov_b32_e32 v44, 0
	v_mov_b32_e32 v45, 0
	s_and_saveexec_b64 s[28:29], s[0:1]
	s_cbranch_execz .LBB3_355
	s_ashr_i32 s27, s22, 31
	s_add_u32 s22, s6, s22
	s_addc_u32 s27, s7, s27
	s_mul_i32 s30, s22, s48
	s_mul_hi_u32 s31, s22, s33
	s_add_i32 s30, s31, s30
	s_mul_i32 s27, s27, s33
	s_add_i32 s31, s30, s27
	s_mul_i32 s30, s22, s33
	s_lshl_b64 s[30:31], s[30:31], 1
	v_lshl_add_u64 v[10:11], v[158:159], 0, s[30:31]
	global_load_dwordx4 v[106:109], v[10:11], off
	v_lshl_add_u64 v[10:11], v[160:161], 0, s[30:31]
	global_load_dwordx4 v[42:45], v[10:11], off
.LBB3_355:
	s_or_b64 exec, exec, s[28:29]
	v_mov_b32_e32 v122, 0
	v_mov_b32_e32 v126, 0
	v_mov_b32_e32 v127, 0
	v_mov_b32_e32 v128, 0
	s_waitcnt lgkmcnt(0)
	v_readfirstlane_b32 s22, v220
	v_mov_b32_e32 v129, 0
	v_mov_b32_e32 v50, 0
	v_mov_b32_e32 v51, 0
	v_mov_b32_e32 v52, 0
	v_mov_b32_e32 v53, 0
	s_and_saveexec_b64 s[28:29], s[0:1]
	s_cbranch_execz .LBB3_357
	s_ashr_i32 s27, s22, 31
	s_add_u32 s22, s6, s22
	s_addc_u32 s27, s7, s27
	s_mul_i32 s30, s22, s48
	s_mul_hi_u32 s31, s22, s33
	s_add_i32 s30, s31, s30
	s_mul_i32 s27, s27, s33
	s_add_i32 s31, s30, s27
	s_mul_i32 s30, s22, s33
	s_lshl_b64 s[30:31], s[30:31], 1
	v_lshl_add_u64 v[10:11], v[158:159], 0, s[30:31]
	global_load_dwordx4 v[126:129], v[10:11], off
	v_lshl_add_u64 v[10:11], v[160:161], 0, s[30:31]
	global_load_dwordx4 v[50:53], v[10:11], off
.LBB3_357:
	s_or_b64 exec, exec, s[28:29]
	v_mov_b32_e32 v123, 0
	v_mov_b32_e32 v124, 0
	v_mov_b32_e32 v125, 0
	v_mov_b32_e32 v58, 0
	s_waitcnt lgkmcnt(0)
	v_readfirstlane_b32 s22, v221
	v_mov_b32_e32 v59, 0
	v_mov_b32_e32 v60, 0
	v_mov_b32_e32 v61, 0
	s_and_saveexec_b64 s[28:29], s[0:1]
	s_cbranch_execz .LBB3_359
	s_ashr_i32 s27, s22, 31
	s_add_u32 s22, s6, s22
	s_addc_u32 s27, s7, s27
	s_mul_i32 s30, s22, s48
	s_mul_hi_u32 s31, s22, s33
	s_add_i32 s30, s31, s30
	s_mul_i32 s27, s27, s33
	s_add_i32 s31, s30, s27
	s_mul_i32 s30, s22, s33
	s_lshl_b64 s[30:31], s[30:31], 1
	v_lshl_add_u64 v[10:11], v[158:159], 0, s[30:31]
	global_load_dwordx4 v[122:125], v[10:11], off
	v_lshl_add_u64 v[10:11], v[160:161], 0, s[30:31]
	global_load_dwordx4 v[58:61], v[10:11], off
.LBB3_359:
	s_or_b64 exec, exec, s[28:29]
	v_mov_b32_e32 v130, 0
	v_mov_b32_e32 v134, 0
	v_mov_b32_e32 v135, 0
	v_mov_b32_e32 v136, 0
	s_waitcnt lgkmcnt(0)
	v_readfirstlane_b32 s22, v222
	v_mov_b32_e32 v137, 0
	v_mov_b32_e32 v66, 0
	v_mov_b32_e32 v67, 0
	v_mov_b32_e32 v68, 0
	v_mov_b32_e32 v69, 0
	s_and_saveexec_b64 s[28:29], s[0:1]
	s_cbranch_execz .LBB3_361
	s_ashr_i32 s27, s22, 31
	s_add_u32 s22, s6, s22
	s_addc_u32 s27, s7, s27
	s_mul_i32 s30, s22, s48
	s_mul_hi_u32 s31, s22, s33
	s_add_i32 s30, s31, s30
	s_mul_i32 s27, s27, s33
	s_add_i32 s31, s30, s27
	s_mul_i32 s30, s22, s33
	s_lshl_b64 s[30:31], s[30:31], 1
	v_lshl_add_u64 v[10:11], v[158:159], 0, s[30:31]
	global_load_dwordx4 v[134:137], v[10:11], off
	v_lshl_add_u64 v[10:11], v[160:161], 0, s[30:31]
	global_load_dwordx4 v[66:69], v[10:11], off
.LBB3_361:
	s_or_b64 exec, exec, s[28:29]
	v_mov_b32_e32 v131, 0
	v_mov_b32_e32 v132, 0
	v_mov_b32_e32 v133, 0
	v_mov_b32_e32 v82, 0
	s_waitcnt lgkmcnt(0)
	v_readfirstlane_b32 s22, v223
	ds_read_b128 v[220:223], v219 offset:32
	v_mov_b32_e32 v83, 0
	v_mov_b32_e32 v84, 0
	v_mov_b32_e32 v85, 0
	s_and_saveexec_b64 s[28:29], s[0:1]
	s_cbranch_execz .LBB3_363
	s_ashr_i32 s27, s22, 31
	s_add_u32 s22, s6, s22
	s_addc_u32 s27, s7, s27
	s_mul_i32 s30, s22, s48
	s_mul_hi_u32 s31, s22, s33
	s_add_i32 s30, s31, s30
	s_mul_i32 s27, s27, s33
	s_add_i32 s31, s30, s27
	s_mul_i32 s30, s22, s33
	s_lshl_b64 s[30:31], s[30:31], 1
	v_lshl_add_u64 v[10:11], v[158:159], 0, s[30:31]
	global_load_dwordx4 v[130:133], v[10:11], off
	v_lshl_add_u64 v[10:11], v[160:161], 0, s[30:31]
	global_load_dwordx4 v[82:85], v[10:11], off
.LBB3_363:
	s_or_b64 exec, exec, s[28:29]
	v_mov_b32_e32 v70, 0
	v_mov_b32_e32 v74, 0
	v_mov_b32_e32 v75, 0
	v_mov_b32_e32 v76, 0
	s_waitcnt lgkmcnt(0)
	v_readfirstlane_b32 s22, v220
	v_mov_b32_e32 v77, 0
	v_mov_b32_e32 v10, 0
	v_mov_b32_e32 v11, 0
	v_mov_b32_e32 v12, 0
	v_mov_b32_e32 v13, 0
	s_and_saveexec_b64 s[28:29], s[0:1]
	s_cbranch_execz .LBB3_365
	s_ashr_i32 s27, s22, 31
	s_add_u32 s22, s6, s22
	s_addc_u32 s27, s7, s27
	s_mul_i32 s30, s22, s48
	s_mul_hi_u32 s31, s22, s33
	s_add_i32 s30, s31, s30
	s_mul_i32 s27, s27, s33
	s_add_i32 s31, s30, s27
	s_mul_i32 s30, s22, s33
	s_lshl_b64 s[30:31], s[30:31], 1
	v_lshl_add_u64 v[10:11], v[158:159], 0, s[30:31]
	global_load_dwordx4 v[74:77], v[10:11], off
	v_lshl_add_u64 v[10:11], v[160:161], 0, s[30:31]
	global_load_dwordx4 v[10:13], v[10:11], off
.LBB3_365:
	s_or_b64 exec, exec, s[28:29]
	v_mov_b32_e32 v71, 0
	v_mov_b32_e32 v72, 0
	v_mov_b32_e32 v73, 0
	v_mov_b32_e32 v14, 0
	s_waitcnt lgkmcnt(0)
	v_readfirstlane_b32 s22, v221
	v_mov_b32_e32 v15, 0
	v_mov_b32_e32 v16, 0
	v_mov_b32_e32 v17, 0
	s_and_saveexec_b64 s[28:29], s[0:1]
	s_cbranch_execz .LBB3_367
	s_ashr_i32 s27, s22, 31
	s_add_u32 s22, s6, s22
	s_addc_u32 s27, s7, s27
	s_mul_i32 s30, s22, s48
	s_mul_hi_u32 s31, s22, s33
	s_add_i32 s30, s31, s30
	s_mul_i32 s27, s27, s33
	s_add_i32 s31, s30, s27
	s_mul_i32 s30, s22, s33
	s_lshl_b64 s[30:31], s[30:31], 1
	v_lshl_add_u64 v[14:15], v[158:159], 0, s[30:31]
	global_load_dwordx4 v[70:73], v[14:15], off
	v_lshl_add_u64 v[14:15], v[160:161], 0, s[30:31]
	global_load_dwordx4 v[14:17], v[14:15], off
.LBB3_367:
	s_or_b64 exec, exec, s[28:29]
	v_mov_b32_e32 v78, 0
	v_mov_b32_e32 v86, 0
	v_mov_b32_e32 v87, 0
	v_mov_b32_e32 v88, 0
	s_waitcnt lgkmcnt(0)
	v_readfirstlane_b32 s22, v222
	v_mov_b32_e32 v89, 0
	v_mov_b32_e32 v22, 0
	v_mov_b32_e32 v23, 0
	v_mov_b32_e32 v24, 0
	v_mov_b32_e32 v25, 0
	s_and_saveexec_b64 s[28:29], s[0:1]
	s_cbranch_execz .LBB3_369
	s_ashr_i32 s27, s22, 31
	s_add_u32 s22, s6, s22
	s_addc_u32 s27, s7, s27
	s_mul_i32 s30, s22, s48
	s_mul_hi_u32 s31, s22, s33
	s_add_i32 s30, s31, s30
	s_mul_i32 s27, s27, s33
	s_add_i32 s31, s30, s27
	s_mul_i32 s30, s22, s33
	s_lshl_b64 s[30:31], s[30:31], 1
	v_lshl_add_u64 v[22:23], v[158:159], 0, s[30:31]
	global_load_dwordx4 v[86:89], v[22:23], off
	v_lshl_add_u64 v[22:23], v[160:161], 0, s[30:31]
	global_load_dwordx4 v[22:25], v[22:23], off
.LBB3_369:
	s_or_b64 exec, exec, s[28:29]
	v_mov_b32_e32 v79, 0
	v_mov_b32_e32 v80, 0
	v_mov_b32_e32 v81, 0
	v_mov_b32_e32 v30, 0
	s_waitcnt lgkmcnt(0)
	v_readfirstlane_b32 s22, v223
	ds_read_b128 v[220:223], v219 offset:48
	v_mov_b32_e32 v31, 0
	v_mov_b32_e32 v32, 0
	v_mov_b32_e32 v33, 0
	s_and_saveexec_b64 s[28:29], s[0:1]
	s_cbranch_execz .LBB3_371
	s_ashr_i32 s27, s22, 31
	s_add_u32 s22, s6, s22
	s_addc_u32 s27, s7, s27
	s_mul_i32 s30, s22, s48
	s_mul_hi_u32 s31, s22, s33
	s_add_i32 s30, s31, s30
	s_mul_i32 s27, s27, s33
	s_add_i32 s31, s30, s27
	s_mul_i32 s30, s22, s33
	s_lshl_b64 s[30:31], s[30:31], 1
	v_lshl_add_u64 v[30:31], v[158:159], 0, s[30:31]
	global_load_dwordx4 v[78:81], v[30:31], off
	v_lshl_add_u64 v[30:31], v[160:161], 0, s[30:31]
	global_load_dwordx4 v[30:33], v[30:31], off
.LBB3_371:
	s_or_b64 exec, exec, s[28:29]
	v_mov_b32_e32 v94, 0
	v_mov_b32_e32 v102, 0
	v_mov_b32_e32 v103, 0
	v_mov_b32_e32 v104, 0
	s_waitcnt lgkmcnt(0)
	v_readfirstlane_b32 s22, v220
	v_mov_b32_e32 v105, 0
	v_mov_b32_e32 v38, 0
	v_mov_b32_e32 v39, 0
	v_mov_b32_e32 v40, 0
	v_mov_b32_e32 v41, 0
	s_and_saveexec_b64 s[28:29], s[0:1]
	s_cbranch_execz .LBB3_373
	s_ashr_i32 s27, s22, 31
	s_add_u32 s22, s6, s22
	s_addc_u32 s27, s7, s27
	s_mul_i32 s30, s22, s48
	s_mul_hi_u32 s31, s22, s33
	s_add_i32 s30, s31, s30
	s_mul_i32 s27, s27, s33
	s_add_i32 s31, s30, s27
	s_mul_i32 s30, s22, s33
	s_lshl_b64 s[30:31], s[30:31], 1
	v_lshl_add_u64 v[38:39], v[158:159], 0, s[30:31]
	global_load_dwordx4 v[102:105], v[38:39], off
	v_lshl_add_u64 v[38:39], v[160:161], 0, s[30:31]
	global_load_dwordx4 v[38:41], v[38:39], off
.LBB3_373:
	s_or_b64 exec, exec, s[28:29]
	v_mov_b32_e32 v95, 0
	v_mov_b32_e32 v96, 0
	v_mov_b32_e32 v97, 0
	v_mov_b32_e32 v46, 0
	s_waitcnt lgkmcnt(0)
	v_readfirstlane_b32 s22, v221
	v_mov_b32_e32 v47, 0
	v_mov_b32_e32 v48, 0
	v_mov_b32_e32 v49, 0
	s_and_saveexec_b64 s[28:29], s[0:1]
	s_cbranch_execz .LBB3_375
	s_ashr_i32 s27, s22, 31
	s_add_u32 s22, s6, s22
	s_addc_u32 s27, s7, s27
	s_mul_i32 s30, s22, s48
	s_mul_hi_u32 s31, s22, s33
	s_add_i32 s30, s31, s30
	s_mul_i32 s27, s27, s33
	s_add_i32 s31, s30, s27
	s_mul_i32 s30, s22, s33
	s_lshl_b64 s[30:31], s[30:31], 1
	v_lshl_add_u64 v[46:47], v[158:159], 0, s[30:31]
	global_load_dwordx4 v[94:97], v[46:47], off
	v_lshl_add_u64 v[46:47], v[160:161], 0, s[30:31]
	global_load_dwordx4 v[46:49], v[46:47], off
.LBB3_375:
	s_or_b64 exec, exec, s[28:29]
	v_mov_b32_e32 v110, 0
	v_mov_b32_e32 v118, 0
	v_mov_b32_e32 v119, 0
	v_mov_b32_e32 v120, 0
	s_waitcnt lgkmcnt(0)
	v_readfirstlane_b32 s22, v222
	v_mov_b32_e32 v121, 0
	v_mov_b32_e32 v54, 0
	v_mov_b32_e32 v55, 0
	v_mov_b32_e32 v56, 0
	v_mov_b32_e32 v57, 0
	s_and_saveexec_b64 s[28:29], s[0:1]
	s_cbranch_execz .LBB3_377
	s_ashr_i32 s27, s22, 31
	s_add_u32 s22, s6, s22
	s_addc_u32 s27, s7, s27
	s_mul_i32 s30, s22, s48
	s_mul_hi_u32 s31, s22, s33
	s_add_i32 s30, s31, s30
	s_mul_i32 s27, s27, s33
	s_add_i32 s31, s30, s27
	s_mul_i32 s30, s22, s33
	s_lshl_b64 s[30:31], s[30:31], 1
	v_lshl_add_u64 v[54:55], v[158:159], 0, s[30:31]
	global_load_dwordx4 v[118:121], v[54:55], off
	v_lshl_add_u64 v[54:55], v[160:161], 0, s[30:31]
	global_load_dwordx4 v[54:57], v[54:55], off
.LBB3_377:
	s_or_b64 exec, exec, s[28:29]
	v_mov_b32_e32 v111, 0
	v_mov_b32_e32 v112, 0
	v_mov_b32_e32 v113, 0
	v_mov_b32_e32 v62, 0
	s_waitcnt lgkmcnt(0)
	v_readfirstlane_b32 s22, v223
	v_mov_b32_e32 v63, 0
	v_mov_b32_e32 v64, 0
	v_mov_b32_e32 v65, 0
	s_and_saveexec_b64 s[28:29], s[0:1]
	s_cbranch_execz .LBB3_379
	s_ashr_i32 s27, s22, 31
	s_add_u32 s6, s6, s22
	s_addc_u32 s7, s7, s27
	s_mul_i32 s22, s6, s48
	s_mul_hi_u32 s27, s6, s33
	s_add_i32 s22, s27, s22
	s_mul_i32 s7, s7, s33
	s_add_i32 s7, s22, s7
	s_mul_i32 s6, s6, s33
	s_lshl_b64 s[6:7], s[6:7], 1
	v_lshl_add_u64 v[62:63], v[158:159], 0, s[6:7]
	global_load_dwordx4 v[110:113], v[62:63], off
	v_lshl_add_u64 v[62:63], v[160:161], 0, s[6:7]
	global_load_dwordx4 v[62:65], v[62:63], off

	.amdhsa_kernel _Z11attn_kernelPKtiS0_iS0_iPti6CoArgs
		.amdhsa_group_segment_fixed_size 83968
		.amdhsa_private_segment_fixed_size 0
		.amdhsa_kernarg_size 176
		.amdhsa_user_sgpr_count 2
		.amdhsa_user_sgpr_dispatch_ptr 0
		.amdhsa_user_sgpr_queue_ptr 0
		.amdhsa_user_sgpr_kernarg_segment_ptr 1
		.amdhsa_user_sgpr_dispatch_id 0
		.amdhsa_user_sgpr_kernarg_preload_length 0
		.amdhsa_user_sgpr_kernarg_preload_offset 0
		.amdhsa_user_sgpr_private_segment_size 0
		.amdhsa_uses_dynamic_stack 0
		.amdhsa_enable_private_segment 0
		.amdhsa_system_sgpr_workgroup_id_x 1
		.amdhsa_system_sgpr_workgroup_id_y 0
		.amdhsa_system_sgpr_workgroup_id_z 0
		.amdhsa_system_sgpr_workgroup_info 0
		.amdhsa_system_vgpr_workitem_id 0
		.amdhsa_next_free_vgpr 224
		.amdhsa_next_free_sgpr 96
		.amdhsa_accum_offset 224
		.amdhsa_reserve_vcc 1
		.amdhsa_float_round_mode_32 0
		.amdhsa_float_round_mode_16_64 0
		.amdhsa_float_denorm_mode_32 3
		.amdhsa_float_denorm_mode_16_64 3
		.amdhsa_dx10_clamp 1
		.amdhsa_ieee_mode 1
		.amdhsa_fp16_overflow 0
		.amdhsa_tg_split 0
		.amdhsa_exception_fp_ieee_invalid_op 0
		.amdhsa_exception_fp_denorm_src 0
		.amdhsa_exception_fp_ieee_div_zero 0
		.amdhsa_exception_fp_ieee_overflow 0
		.amdhsa_exception_fp_ieee_underflow 0
		.amdhsa_exception_fp_ieee_inexact 0
		.amdhsa_exception_int_div_zero 0
	.end_amdhsa_kernel

amdhsa.kernels:
  - .agpr_count:     0
    .args:
      - .offset:         0
        .size:           4
        .value_kind:     by_value
      - .actual_access:  read_only
        .address_space:  global
        .offset:         8
        .size:           8
        .value_kind:     global_buffer
      - .actual_access:  read_only
        .address_space:  global
        .offset:         16
        .size:           8
        .value_kind:     global_buffer
      - .actual_access:  read_only
        .address_space:  global
        .offset:         24
        .size:           8
        .value_kind:     global_buffer
      - .actual_access:  read_only
        .address_space:  global
        .offset:         32
        .size:           8
        .value_kind:     global_buffer
      - .offset:         40
        .size:           4
        .value_kind:     by_value
      - .actual_access:  read_only
        .address_space:  global
        .offset:         48
        .size:           8
        .value_kind:     global_buffer
      - .actual_access:  read_only
        .address_space:  global
        .offset:         56
        .size:           8
        .value_kind:     global_buffer
      - .offset:         64
        .size:           4
        .value_kind:     by_value
      - .actual_access:  write_only
        .address_space:  global
        .offset:         72
        .size:           8
        .value_kind:     global_buffer
      - .offset:         80
        .size:           4
        .value_kind:     by_value
    .group_segment_fixed_size: 128
    .kernarg_segment_align: 8
    .kernarg_segment_size: 84
    .language:       OpenCL C
    .language_version:
      - 2
      - 0
    .max_flat_workgroup_size: 256
    .name:           _Z12graph_kerneliPKfS0_S0_PKtiS2_S2_iPti
    .private_segment_fixed_size: 0
    .sgpr_count:     48
    .sgpr_spill_count: 0
    .symbol:         _Z12graph_kerneliPKfS0_S0_PKtiS2_S2_iPti.kd
    .uniform_work_group_size: 1
    .uses_dynamic_stack: false
    .vgpr_count:     75
    .vgpr_spill_count: 0
    .wavefront_size: 64
  - .agpr_count:     0
    .args:
      - .offset:         0
        .size:           96
        .value_kind:     by_value
      - .offset:         96
        .size:           336
        .value_kind:     by_value
      - .offset:         432
        .size:           328
        .value_kind:     by_value
    .group_segment_fixed_size: 50688
    .kernarg_segment_align: 8
    .kernarg_segment_size: 760
    .language:       OpenCL C
    .language_version:
      - 2
      - 0
    .max_flat_workgroup_size: 512
    .name:           _Z12front_kernel9FrontArgs8PrepArgs8FragArgs
    .private_segment_fixed_size: 0
    .sgpr_count:     58
    .sgpr_spill_count: 0
    .symbol:         _Z12front_kernel9FrontArgs8PrepArgs8FragArgs.kd
    .uniform_work_group_size: 1
    .uses_dynamic_stack: false
    .vgpr_count:     80
    .vgpr_spill_count: 0
    .wavefront_size: 64
  - .agpr_count:     0
    .args:
      - .offset:         0
        .size:           144
        .value_kind:     by_value
    .group_segment_fixed_size: 131072
    .kernarg_segment_align: 8
    .kernarg_segment_size: 144
    .language:       OpenCL C
    .language_version:
      - 2
      - 0
    .max_flat_workgroup_size: 512
    .name:           _Z13gemm8p_kernel5GArgs
    .private_segment_fixed_size: 0
    .sgpr_count:     42
    .sgpr_spill_count: 0
    .symbol:         _Z13gemm8p_kernel5GArgs.kd
    .uniform_work_group_size: 1
    .uses_dynamic_stack: false
    .vgpr_count:     250
    .vgpr_spill_count: 0
    .wavefront_size: 64
  - .agpr_count:     0
    .args:
      - .actual_access:  read_only
        .address_space:  global
        .offset:         0
        .size:           8
        .value_kind:     global_buffer
      - .offset:         8
        .size:           4
        .value_kind:     by_value
      - .address_space:  global
        .offset:         16
        .size:           8
        .value_kind:     global_buffer
      - .offset:         24
        .size:           4
        .value_kind:     by_value
      - .address_space:  global
        .offset:         32
        .size:           8
        .value_kind:     global_buffer
      - .offset:         40
        .size:           4
        .value_kind:     by_value
      - .actual_access:  write_only
        .address_space:  global
        .offset:         48
        .size:           8
        .value_kind:     global_buffer
      - .offset:         56
        .size:           4
        .value_kind:     by_value
      - .offset:         64
        .size:           112
        .value_kind:     by_value
    .group_segment_fixed_size: 83968
    .kernarg_segment_align: 8
    .kernarg_segment_size: 176
    .language:       OpenCL C
    .language_version:
      - 2
      - 0
    .max_flat_workgroup_size: 512
    .name:           _Z11attn_kernelPKtiS0_iS0_iPti6CoArgs
    .private_segment_fixed_size: 0
    .sgpr_count:     74
    .sgpr_spill_count: 0
    .symbol:         _Z11attn_kernelPKtiS0_iS0_iPti6CoArgs.kd
    .uniform_work_group_size: 1
    .uses_dynamic_stack: false
    .vgpr_count:     224
    .vgpr_spill_count: 0
    .wavefront_size: 64
  - .agpr_count:     0
    .args:
      - .offset:         0
        .size:           144
        .value_kind:     by_value
    .group_segment_fixed_size: 77312
    .kernarg_segment_align: 8
    .kernarg_segment_size: 144
    .language:       OpenCL C
    .language_version:
      - 2
      - 0
    .max_flat_workgroup_size: 512
    .name:           _Z12chain_kernelILi0EEv9ChainArgs
    .private_segment_fixed_size: 0
    .sgpr_count:     35
    .sgpr_spill_count: 0
    .symbol:         _Z12chain_kernelILi0EEv9ChainArgs.kd
    .uniform_work_group_size: 1
    .uses_dynamic_stack: false
    .vgpr_count:     224
    .vgpr_spill_count: 0
    .wavefront_size: 64
  - .agpr_count:     0
    .args:
      - .offset:         0
        .size:           144
        .value_kind:     by_value
    .group_segment_fixed_size: 77312
    .kernarg_segment_align: 8
    .kernarg_segment_size: 144
    .language:       OpenCL C
    .language_version:
      - 2
      - 0
    .max_flat_workgroup_size: 512
    .name:           _Z12chain_kernelILi1EEv9ChainArgs
    .private_segment_fixed_size: 0
    .sgpr_count:     35
    .sgpr_spill_count: 0
    .symbol:         _Z12chain_kernelILi1EEv9ChainArgs.kd
    .uniform_work_group_size: 1
    .uses_dynamic_stack: false
    .vgpr_count:     210
    .vgpr_spill_count: 0
    .wavefront_size: 64
